# upsample: four output stores issued as soon as their data is final (before the loss-reduction chain), vmcnt waits recounted
# speedup vs baseline: 1.0073x; 1.0001x over previous
_Z10k_upsamplePKfS0_PfS1_:
	s_ashr_i32 s5, s4, 31
	s_load_dwordx4 s[8:11], s[0:1], 0x0
	s_load_dwordx2 s[6:7], s[0:1], 0x10
	s_lshl_b64 s[12:13], s[4:5], 6
	s_ashr_i32 s5, s3, 31
	v_lshrrev_b32_e32 v1, 6, v0
	s_add_u32 s12, s12, s3
	v_lshl_or_b32 v19, s2, 2, v1
	s_addc_u32 s13, s13, s5
	v_and_b32_e32 v29, 63, v0
	s_lshl_b64 s[14:15], s[12:13], 14
	v_max_i32_e32 v2, 1, v19
	v_not_b32_e32 v3, 63
	s_waitcnt lgkmcnt(0)
	s_add_u32 s8, s8, s14
	v_sub_u32_e64 v14, v29, 1 clamp
	v_lshl_add_u32 v8, v2, 6, v3
	s_addc_u32 s9, s9, s15
	v_min_i32_e32 v15, 62, v19
	v_or_b32_e32 v2, v14, v8
	v_mov_b32_e32 v3, 0
	v_min_u32_e32 v21, 62, v29
	v_lshl_add_u64 v[4:5], v[2:3], 2, s[8:9]
	v_or_b32_e32 v2, v8, v29
	v_lshlrev_b32_e32 v12, 6, v19
	v_lshl_add_u32 v23, v15, 6, 64
	v_lshl_add_u64 v[6:7], v[2:3], 2, s[8:9]
	v_or_b32_e32 v2, v21, v8
	v_or_b32_e32 v8, v14, v12
	v_or_b32_e32 v10, v12, v29
	v_or_b32_e32 v14, v14, v23
	v_or_b32_e32 v16, v23, v29
	v_lshl_add_u64 v[2:3], v[2:3], 2, s[8:9]
	v_ashrrev_i32_e32 v9, 31, v8
	v_ashrrev_i32_e32 v11, 31, v10
	v_ashrrev_i32_e32 v13, 31, v12
	v_or_b32_e32 v12, v12, v21
	v_ashrrev_i32_e32 v15, 31, v14
	v_ashrrev_i32_e32 v17, 31, v16
	v_lshl_add_u64 v[8:9], v[8:9], 2, s[8:9]
	v_lshl_add_u64 v[10:11], v[10:11], 2, s[8:9]
	v_lshl_add_u64 v[12:13], v[12:13], 2, s[8:9]
	v_lshl_add_u64 v[14:15], v[14:15], 2, s[8:9]
	v_lshl_add_u64 v[16:17], v[16:17], 2, s[8:9]
	global_load_dword v18, v[4:5], off
	global_load_dword v20, v[6:7], off
	global_load_dword v25, v[2:3], off offset:4
	global_load_dword v22, v[8:9], off
	global_load_dword v24, v[10:11], off
	global_load_dword v27, v[12:13], off offset:4
	global_load_dword v26, v[14:15], off
	global_load_dword v28, v[16:17], off
	v_ashrrev_i32_e32 v3, 31, v23
	v_or_b32_e32 v2, v23, v21
	v_lshl_add_u64 v[2:3], v[2:3], 2, s[8:9]
	global_load_dword v21, v[2:3], off offset:4
	v_lshlrev_b32_e32 v2, 2, v19
	v_ashrrev_i32_e32 v3, 31, v2
	s_lshl_b64 s[8:9], s[12:13], 16
	v_lshlrev_b64 v[2:3], 8, v[2:3]
	v_lshl_add_u64 v[2:3], v[2:3], 0, s[8:9]
	v_lshl_or_b32 v2, v29, 2, v2
	v_lshlrev_b64 v[30:31], 2, v[2:3]
	v_lshl_add_u64 v[32:33], s[10:11], 0, v[30:31]
	global_load_dwordx4 v[2:5], v[32:33], off
	global_load_dwordx4 v[6:9], v[32:33], off offset:1024
	global_load_dwordx4 v[10:13], v[32:33], off offset:2048
	global_load_dwordx4 v[14:17], v[32:33], off offset:3072
	s_mov_b32 s8, 0x3f200000
	s_mov_b32 s9, 0x3f600000
	s_mov_b32 s10, 0x3e000000
	s_mov_b32 s11, 0x3ec00000
	s_mov_b32 s12, s9
	s_waitcnt vmcnt(11)
	v_sub_f32_e32 v32, v20, v18
	v_pk_fma_f32 v[32:33], v[32:33], s[8:9], v[18:19] op_sel_hi:[0,1,0]
	s_waitcnt vmcnt(10)
	v_sub_f32_e32 v34, v25, v20
	s_waitcnt vmcnt(8)
	v_sub_f32_e32 v36, v24, v22
	v_pk_fma_f32 v[36:37], v[36:37], s[8:9], v[22:23] op_sel_hi:[0,1,0]
	s_waitcnt vmcnt(7)
	v_sub_f32_e32 v38, v27, v24
	v_pk_add_f32 v[22:23], v[36:37], v[32:33] neg_lo:[0,1] neg_hi:[0,1]
	v_pk_fma_f32 v[38:39], v[38:39], s[10:11], v[24:25] op_sel_hi:[0,1,0]
	v_pk_fma_f32 v[18:19], v[22:23], s[8:9], v[32:33] op_sel_hi:[1,0,1]
	v_pk_fma_f32 v[22:23], v[22:23], s[12:13], v[32:33] op_sel_hi:[1,0,1]
	s_waitcnt vmcnt(4)
	v_pk_fma_f32 v[34:35], v[34:35], s[10:11], v[20:21] op_sel_hi:[0,1,0]
	v_pk_add_f32 v[24:25], v[38:39], v[34:35] neg_lo:[0,1] neg_hi:[0,1]
	v_sub_f32_e32 v42, v21, v28
	v_pk_fma_f32 v[20:21], v[24:25], s[8:9], v[34:35] op_sel_hi:[1,0,1]
	v_pk_fma_f32 v[24:25], v[24:25], s[12:13], v[34:35] op_sel_hi:[1,0,1]
	v_sub_f32_e32 v40, v28, v26
	v_lshl_add_u64 v[32:33], s[6:7], 0, v[30:31]
	global_store_dwordx4 v[32:33], v[18:21], off
	global_store_dwordx4 v[32:33], v[22:25], off offset:1024
	s_waitcnt vmcnt(5)
	v_sub_f32_e32 v3, v19, v3
	v_sub_f32_e32 v2, v18, v2
	v_mul_f32_e32 v3, v3, v3
	v_sub_f32_e32 v4, v20, v4
	v_fmac_f32_e32 v3, v2, v2
	v_fmac_f32_e32 v3, v4, v4
	s_waitcnt vmcnt(4)
	v_sub_f32_e32 v4, v23, v7
	v_sub_f32_e32 v5, v21, v5
	v_sub_f32_e32 v2, v22, v6
	v_mul_f32_e32 v4, v4, v4
	v_fmac_f32_e32 v3, v5, v5
	v_sub_f32_e32 v5, v24, v8
	v_fmac_f32_e32 v4, v2, v2
	v_sub_f32_e32 v6, v25, v9
	v_fmac_f32_e32 v4, v5, v5
	v_fmac_f32_e32 v4, v6, v6
	v_add_f32_e32 v8, v3, v4
	v_pk_fma_f32 v[2:3], v[40:41], s[8:9], v[26:27] op_sel_hi:[0,1,0]
	v_pk_add_f32 v[2:3], v[2:3], v[36:37] neg_lo:[0,1] neg_hi:[0,1]
	v_pk_fma_f32 v[6:7], v[42:43], s[10:11], v[28:29] op_sel_hi:[0,1,0]
	v_pk_fma_f32 v[4:5], v[2:3], s[10:11], v[36:37] op_sel_hi:[1,0,1]
	v_pk_add_f32 v[26:27], v[6:7], v[38:39] neg_lo:[0,1] neg_hi:[0,1]
	s_waitcnt vmcnt(3)
	v_sub_f32_e32 v9, v4, v10
	v_sub_f32_e32 v10, v5, v11
	v_pk_fma_f32 v[6:7], v[26:27], s[10:11], v[38:39] op_sel_hi:[1,0,1]
	global_store_dwordx4 v[32:33], v[4:7], off offset:2048
	v_mul_f32_e32 v10, v10, v10
	v_sub_f32_e32 v11, v6, v12
	v_fmac_f32_e32 v10, v9, v9
	v_sub_f32_e32 v12, v7, v13
	v_fmac_f32_e32 v10, v11, v11
	v_fmac_f32_e32 v10, v12, v12
	s_mov_b32 s8, s11
	v_add_f32_e32 v12, v8, v10
	v_pk_fma_f32 v[8:9], v[2:3], s[8:9], v[36:37] op_sel_hi:[1,0,1]
	v_pk_fma_f32 v[10:11], v[26:27], s[8:9], v[38:39] op_sel_hi:[1,0,1]
	global_store_dwordx4 v[32:33], v[8:11], off offset:3072
	s_waitcnt vmcnt(4)
	v_sub_f32_e32 v3, v9, v15
	v_sub_f32_e32 v2, v8, v14
	v_mul_f32_e32 v3, v3, v3
	v_sub_f32_e32 v13, v10, v16
	v_fmac_f32_e32 v3, v2, v2
	v_sub_f32_e32 v14, v11, v17
	v_fmac_f32_e32 v3, v13, v13
	v_fmac_f32_e32 v3, v14, v14
	v_add_f32_e32 v2, v12, v3
	v_mbcnt_lo_u32_b32 v3, -1, 0
	v_mbcnt_hi_u32_b32 v3, -1, v3
	v_and_b32_e32 v12, 64, v3
	v_add_u32_e32 v14, 64, v12
	v_xor_b32_e32 v12, 32, v3
	v_cmp_lt_i32_e32 vcc, v12, v14
	s_nop 1
	v_cndmask_b32_e32 v12, v3, v12, vcc
	v_lshlrev_b32_e32 v12, 2, v12
	ds_bpermute_b32 v12, v12, v2
	s_waitcnt lgkmcnt(0)
	v_add_f32_e32 v2, v2, v12
	v_xor_b32_e32 v12, 16, v3
	v_cmp_lt_i32_e32 vcc, v12, v14
	s_nop 1
	v_cndmask_b32_e32 v12, v3, v12, vcc
	v_lshlrev_b32_e32 v12, 2, v12
	ds_bpermute_b32 v12, v12, v2
	s_waitcnt lgkmcnt(0)
	v_add_f32_e32 v2, v2, v12
	v_xor_b32_e32 v12, 8, v3
	v_cmp_lt_i32_e32 vcc, v12, v14
	s_nop 1
	v_cndmask_b32_e32 v12, v3, v12, vcc
	v_lshlrev_b32_e32 v12, 2, v12
	ds_bpermute_b32 v12, v12, v2
	s_waitcnt lgkmcnt(0)
	v_add_f32_e32 v2, v2, v12
	v_xor_b32_e32 v12, 4, v3
	v_cmp_lt_i32_e32 vcc, v12, v14
	s_nop 1
	v_cndmask_b32_e32 v12, v3, v12, vcc
	v_lshlrev_b32_e32 v12, 2, v12
	ds_bpermute_b32 v12, v12, v2
	s_waitcnt lgkmcnt(0)
	v_add_f32_e32 v2, v2, v12
	v_xor_b32_e32 v12, 2, v3
	v_cmp_lt_i32_e32 vcc, v12, v14
	s_nop 1
	v_cndmask_b32_e32 v12, v3, v12, vcc
	v_lshlrev_b32_e32 v12, 2, v12
	ds_bpermute_b32 v15, v12, v2
	s_waitcnt lgkmcnt(0)
	v_add_f32_e32 v2, v2, v15
	v_xor_b32_e32 v15, 1, v3
	v_cmp_lt_i32_e32 vcc, v15, v14
	s_nop 1
	v_cndmask_b32_e32 v3, v3, v15, vcc
	v_lshlrev_b32_e32 v3, 2, v3
	ds_bpermute_b32 v3, v3, v2
	v_cmp_eq_u32_e32 vcc, 0, v29
	s_and_saveexec_b64 s[6:7], vcc
	s_cbranch_execz .LBB2_2
	s_waitcnt lgkmcnt(0)
	v_add_f32_e32 v2, v2, v3
	v_lshlrev_b32_e32 v1, 2, v1
	ds_write_b32 v1, v2
